# baseline (speedup 1.0000x reference)
_Z6k_dlrmPKiS0_S0_S0_S0_S0_S0_PKfS2_S2_S2_S2_S2_S2_S2_S2_S2_S2_S2_S2_S2_S2_S2_Pf:
	v_readfirstlane_b32 s33, v0
	s_load_dwordx16 s[40:55], s[0:1], 0x0
	s_load_dwordx16 s[56:71], s[0:1], 0x40
	s_load_dwordx16 s[72:87], s[0:1], 0x80
	s_lshr_b32 s37, s33, 6
	s_lshl_b32 s30, s2, 6
	s_lshl_b32 s34, s37, 2
	v_and_b32_e32 v1, 63, v0
	s_add_i32 s6, s34, s30
	v_lshlrev_b32_e32 v2, 2, v1
	v_lshl_add_u32 v2, s6, 6, v2
	v_ashrrev_i32_e32 v3, 31, v2
	v_and_b32_e32 v17, 31, v0
	v_and_b32_e32 v82, 15, v0
	s_waitcnt lgkmcnt(0)
	s_load_dword s88, s[84:85], 0x0
	v_lshl_add_u64 v[2:3], v[2:3], 2, s[50:51]
	global_load_dwordx4 v[28:31], v[2:3], off nt
	v_lshl_or_b32 v2, s6, 3, v17
	v_ashrrev_i32_e32 v3, 31, v2
	v_lshl_add_u64 v[2:3], v[2:3], 2, s[46:47]
	global_load_dword v13, v[2:3], off nt
	v_cmp_gt_u32_e32 vcc, 4, v1
	v_mov_b32_e32 v15, 0
	v_mov_b32_e32 v5, 0
	v_mov_b32_e32 v4, 0
	v_mov_b32_e32 v3, 0
	v_mov_b32_e32 v2, 0
	s_and_saveexec_b64 s[2:3], vcc
	v_or_b32_e32 v2, s6, v1
	v_ashrrev_i32_e32 v3, 31, v2
	v_lshlrev_b64 v[6:7], 2, v[2:3]
	v_lshl_add_u64 v[2:3], s[52:53], 0, v[6:7]
	v_lshl_add_u64 v[4:5], s[48:49], 0, v[6:7]
	global_load_dword v2, v[2:3], off nt
	v_lshl_add_u64 v[8:9], s[42:43], 0, v[6:7]
	global_load_dword v3, v[4:5], off nt
	v_lshl_add_u64 v[4:5], s[40:41], 0, v[6:7]
	v_lshl_add_u64 v[6:7], s[44:45], 0, v[6:7]
	global_load_dword v4, v[4:5], off nt
	s_nop 0
	global_load_dword v5, v[8:9], off nt
	global_load_dword v15, v[6:7], off nt
	s_or_b64 exec, exec, s[2:3]
	v_or_b32_e32 v6, s30, v1
	v_ashrrev_i32_e32 v7, 31, v6
	v_lshl_add_u64 v[6:7], v[6:7], 2, s[54:55]
	global_load_dword v16, v[6:7], off nt
	s_cmp_lt_u32 s37, 4
	s_cbranch_scc1 .Lpro_wl_done
	v_lshrrev_b32_e32 v20, 5, v1
	v_lshlrev_b32_e32 v21, 2, v17
	v_lshl_or_b32 v22, v20, 12, v21
	v_lshl_or_b32 v23, v20, 10, v21
	v_lshrrev_b32_e32 v24, 4, v1
	v_lshlrev_b32_e32 v25, 2, v82
	v_lshl_or_b32 v24, v24, 11, v25
	v_lshlrev_b32_e32 v26, 2, v1
	s_sub_i32 s89, s37, 4
	s_mul_i32 s90, s89, 13
	s_lshr_b32 s90, s90, 6
	s_mul_i32 s91, s90, 5
	s_sub_i32 s91, s89, s91
	s_lshl_b32 s38, s91, 4
	s_add_i32 s38, s38, 15
	s_cmp_lt_u32 s91, 4
	s_cselect_b32 s38, s38, 0
	s_mov_b32 s92, 0
	s_cselect_b32 s93, 0, -1
	s_lshl_b32 s38, s38, 9
	s_lshl_b32 s90, s90, 7
	s_add_u32 s38, s38, s90
	s_add_u32 s90, s74, s38
	s_addc_u32 s91, s75, 0
	global_load_dword v84, v22, s[90:91]
	global_load_dword v85, v22, s[90:91] offset:512
	global_load_dword v86, v22, s[90:91] offset:1024
	global_load_dword v87, v22, s[90:91] offset:1536
	global_load_dword v88, v22, s[90:91] offset:2048
	global_load_dword v89, v22, s[90:91] offset:2560
	global_load_dword v90, v22, s[90:91] offset:3072
	global_load_dword v91, v22, s[90:91] offset:3584
	s_cmp_lt_u32 s37, 12
	s_cbranch_scc0 .Lpro_r1_w2
	s_add_i32 s89, s37, 8
	s_mul_i32 s90, s89, 13
	s_lshr_b32 s90, s90, 6
	s_mul_i32 s91, s90, 5
	s_sub_i32 s91, s89, s91
	s_lshl_b32 s38, s91, 4
	s_add_i32 s38, s38, 15
	s_cmp_lt_u32 s91, 4
	s_cselect_b32 s38, s38, 0
	s_mov_b32 s94, 0
	s_cselect_b32 s95, 0, -1
	s_lshl_b32 s38, s38, 9
	s_lshl_b32 s90, s90, 7
	s_add_u32 s38, s38, s90
	s_add_u32 s90, s74, s38
	s_addc_u32 s91, s75, 0
	global_load_dword v92, v22, s[90:91]
	global_load_dword v93, v22, s[90:91] offset:512
	global_load_dword v94, v22, s[90:91] offset:1024
	global_load_dword v95, v22, s[90:91] offset:1536
	global_load_dword v96, v22, s[90:91] offset:2048
	global_load_dword v97, v22, s[90:91] offset:2560
	global_load_dword v98, v22, s[90:91] offset:3072
	global_load_dword v99, v22, s[90:91] offset:3584
	s_branch .Lpro_r1_done

.Lpro_not_w0:
	v_cmp_gt_u32_e32 vcc, 4, v1
	s_lshl_b32 s6, s37, 10
	v_lshlrev_b32_e32 v6, 6, v0
	s_lshl_b32 s7, s37, 7
	s_add_i32 s6, s6, 0xf400
	v_and_b32_e32 v6, 0xc0, v6
	v_and_b32_e32 v7, 60, v1
	s_lshl_b32 s31, s37, 5
	s_add_i32 s7, s7, 0x13c00
	v_lshrrev_b32_e32 v7, 4, v1
	v_lshlrev_b32_e32 v7, 8, v7
	v_lshl_or_b32 v6, v82, 2, v7
	v_add_u32_e32 v6, s6, v6
	v_cmp_gt_u32_e64 s[2:3], 32, v1
	ds_write2_b32 v6, v28, v29 offset1:16
	ds_write2_b32 v6, v30, v31 offset0:32 offset1:48
	s_and_saveexec_b64 s[4:5], s[2:3]
	v_lshl_add_u32 v6, v1, 2, s7
	ds_write_b32 v6, v13
	s_or_b64 exec, exec, s[4:5]
	s_mov_b64 s[14:15], s[60:61]
	s_mov_b64 s[24:25], s[56:57]
	s_mov_b64 s[26:27], s[58:59]
	s_lshl_b32 s8, s31, 2
	s_add_i32 s8, s8, 0x14400
	s_and_saveexec_b64 s[2:3], vcc
	s_cbranch_execz .LBB0_32
	v_lshl_add_u32 v6, v1, 5, s8
	ds_write_b128 v6, v[2:5]
	ds_write_b32 v6, v15 offset:16
